# scan balance: delta-rule workgroups' SEQ Hyena unit runs on the GLA workgroups (second pass of their specialised unit code), GLA workgroups' last 8 conversion items moved to the out-projection tail
# baseline (speedup 1.0000x reference)
; #define LAS __attribute__((address_space(3)))
; __device__ __forceinline__ int tidx() { int t = threadIdx.x; asm volatile("" : "+v"(t)); return t; }
; template <int L>
; __device__ __forceinline__ void hyena_unit(CArgs& a, int l, int c, LAS unsigned char* lds) {
;     constexpr int Lt = L == SEQ ? 1 : 0, SOFF = L == SEQ ? CTXL : 0, CST = (2 * L + 16) * 2 + 32;
;     constexpr int NTW = L / 16 / 8;
;     const int tid = tidx(), lane = tid & 63, w = tid >> 6, fr = lane & 15, kg = lane >> 4;
;     const float* kf = (const float*)(a.ws + WS_KUN) + ((size_t)((l * 2 + Lt) * 512 + c)) * 2048;
;     const float* kb = kf + (size_t)256 * 2048;
;     LAS float* red = (LAS float*)(lds + 8 * CST);
;     const bf16* Z = (const bf16*)(a.ws + WS_MIX + MX_ZT) + ((size_t)(c * 16 + fr)) * 2304 + SOFF;
;     const bf16* zp = Z + 8 * kg;
;     bf16x8 zc[8];
; #pragma unroll
;     for (int ii = 0; ii < 8; ++ii) zc[ii] = *(const bf16x8*)(zp + 32 * ii);
.Lhy2_again:
	v_readlane_b32 s0, v249, 0
	v_readlane_b32 s1, v249, 1
	s_load_dwordx2 s[2:3], s[0:1], 0x140
	s_lshl_b32 s8, s84, 10
	v_readlane_b32 s0, v252, 20
	s_add_i32 s0, s0, s8
	s_ashr_i32 s1, s0, 31
	s_lshl_b64 s[4:5], s[0:1], 13
	v_readlane_b32 s0, v252, 18
	v_readlane_b32 s1, v252, 19
	s_and_b64 vcc, exec, s[0:1]
	s_cbranch_vccz .LBB0_2273
; #define LAS __attribute__((address_space(3)))
; __device__ __forceinline__ int tidx() { int t = threadIdx.x; asm volatile("" : "+v"(t)); return t; }
; template <int L>
; __device__ __forceinline__ void hyena_unit(CArgs& a, int l, int c, LAS unsigned char* lds) {
;     ...
;     const int tid = tidx(), lane = tid & 63, w = tid >> 6, fr = lane & 15, kg = lane >> 4;
;     const float* kf = (const float*)(a.ws + WS_KUN) + ((size_t)((l * 2 + Lt) * 512 + c)) * 2048;
;     const float* kb = kf + (size_t)256 * 2048;
;     LAS float* red = (LAS float*)(lds + 8 * CST);
;     const bf16* Z = (const bf16*)(a.ws + WS_MIX + MX_ZT) + ((size_t)(c * 16 + fr)) * 2304 + SOFF;
;     const bf16* zp = Z + 8 * kg;
;     bf16x8 zc[8];
; #pragma unroll
;     for (int ii = 0; ii < 8; ++ii) zc[ii] = *(const bf16x8*)(zp + 32 * ii);
;     constexpr int NI = (2 * L + 16 + 511) / 512;
;     float gv[NI];
;     float s = 0.f;
; #pragma unroll
;     for (int q = 0; q < NI; ++q) {
;         const int idx = tid + 512 * q, ic = min(max(idx, 1), 2 * L - 1);
;         const float v = *(ic <= L ? kf + (L - ic) : kb + (ic - L));
;         gv[q] = (idx >= 1 && idx < 2 * L) ? v : 0.f;
;         s += fabsf(gv[q]);
;     }
;     s = wave_sum(s);
;     if (lane == 0) red[w] = s;
	s_waitcnt vmcnt(0)
	v_mov_b32_e32 v37, v0
	v_readlane_b32 s0, v252, 25
	v_and_b32_e32 v36, 15, v37
	s_waitcnt vmcnt(0) lgkmcnt(0)
	v_mov_b64_e32 v[2:3], s[2:3]
	v_or_b32_e32 v1, s0, v36
	s_movk_i32 s0, 0x1200
	v_mad_u64_u32 v[156:157], s[0:1], v1, s0, v[2:3]
	v_and_b32_e32 v34, 48, v37
	v_lshl_add_u64 v[2:3], v[156:157], 0, v[34:35]
	s_mov_b64 s[0:1], 0x4f000200
	v_lshl_add_u64 v[158:159], v[2:3], 0, s[0:1]
	s_add_u32 s0, s2, 0x400000
	s_addc_u32 s1, s3, 0
	s_add_u32 s6, s0, s4
	v_med3_i32 v1, v37, 1, v198
	s_addc_u32 s7, s1, s5
	v_sub_u32_e32 v34, 0x800, v1
	v_lshl_add_u64 v[4:5], v[34:35], 2, s[6:7]
	v_lshlrev_b32_e32 v34, 2, v1
	v_lshl_add_u64 v[6:7], s[6:7], 0, v[34:35]
	s_mov_b64 s[10:11], 0x1fe000
	s_movk_i32 s9, 0x801
	v_lshl_add_u64 v[6:7], v[6:7], 0, s[10:11]
	v_cmp_gt_i32_e32 vcc, s9, v37
	v_add_u32_e32 v52, 0x200, v37
	s_movk_i32 s9, 0x601
	v_cndmask_b32_e32 v4, v6, v4, vcc
	v_med3_i32 v6, v52, 1, v198
	v_cndmask_b32_e32 v5, v7, v5, vcc
	v_sub_u32_e32 v34, 0x800, v6
	global_load_dword v1, v[4:5], off
	v_lshl_add_u64 v[4:5], v[34:35], 2, s[6:7]
	v_lshlrev_b32_e32 v34, 2, v6
	v_lshl_add_u64 v[6:7], s[6:7], 0, v[34:35]
	v_lshl_add_u64 v[6:7], v[6:7], 0, s[10:11]
	v_cmp_gt_i32_e32 vcc, s9, v37
	v_add_u32_e32 v50, 0x400, v37
	s_movk_i32 s9, 0x401
	v_cndmask_b32_e32 v4, v6, v4, vcc
	v_med3_i32 v6, v50, 1, v198
	v_cndmask_b32_e32 v5, v7, v5, vcc
	v_sub_u32_e32 v34, 0x800, v6
	global_load_dword v39, v[4:5], off
	v_lshl_add_u64 v[4:5], v[34:35], 2, s[6:7]
	v_lshlrev_b32_e32 v34, 2, v6
	v_lshl_add_u64 v[6:7], s[6:7], 0, v[34:35]
	v_lshl_add_u64 v[6:7], v[6:7], 0, s[10:11]
	v_cmp_gt_i32_e32 vcc, s9, v37
	v_add_u32_e32 v48, 0x600, v37
	s_movk_i32 s9, 0x201
	v_cndmask_b32_e32 v4, v6, v4, vcc
	v_med3_i32 v6, v48, 1, v198
	v_cndmask_b32_e32 v5, v7, v5, vcc
	v_sub_u32_e32 v34, 0x800, v6
	global_load_dword v41, v[4:5], off
	v_lshl_add_u64 v[4:5], v[34:35], 2, s[6:7]
	v_lshlrev_b32_e32 v34, 2, v6
	v_lshl_add_u64 v[6:7], s[6:7], 0, v[34:35]
	v_lshl_add_u64 v[6:7], v[6:7], 0, s[10:11]
	v_cmp_gt_i32_e32 vcc, s9, v37
	v_add_u32_e32 v46, 0x800, v37
	v_add_u32_e32 v44, 0xa00, v37
	v_cndmask_b32_e32 v4, v6, v4, vcc
	v_med3_i32 v6, v46, 1, v198
	v_cndmask_b32_e32 v5, v7, v5, vcc
	v_sub_u32_e32 v34, 0x800, v6
	global_load_dword v43, v[4:5], off
	v_lshl_add_u64 v[4:5], v[34:35], 2, s[6:7]
	v_lshlrev_b32_e32 v34, 2, v6
	v_lshl_add_u64 v[6:7], s[6:7], 0, v[34:35]
	v_lshl_add_u64 v[6:7], v[6:7], 0, s[10:11]
	v_cmp_gt_i32_e32 vcc, 1, v37
	v_add_u32_e32 v42, 0xc00, v37
	s_movk_i32 s9, 0xfc01
	v_cndmask_b32_e32 v4, v6, v4, vcc
	v_med3_i32 v6, v44, 1, v198
	v_cndmask_b32_e32 v5, v7, v5, vcc
	v_sub_u32_e32 v34, 0x800, v6
	global_load_dword v45, v[4:5], off
	v_lshl_add_u64 v[4:5], v[34:35], 2, s[6:7]
	v_lshlrev_b32_e32 v34, 2, v6
	v_lshl_add_u64 v[6:7], s[6:7], 0, v[34:35]
	v_lshl_add_u64 v[6:7], v[6:7], 0, s[10:11]
	v_cmp_gt_i32_e32 vcc, s36, v37
	v_add_u32_e32 v40, 0xe00, v37
	v_add_u32_e32 v38, 0x1000, v37
	v_cndmask_b32_e32 v4, v6, v4, vcc
	v_med3_i32 v6, v42, 1, v198
	v_cndmask_b32_e32 v5, v7, v5, vcc
	v_sub_u32_e32 v34, 0x800, v6
	global_load_dword v47, v[4:5], off
	v_lshl_add_u64 v[4:5], v[34:35], 2, s[6:7]
	v_lshlrev_b32_e32 v34, 2, v6
	v_lshl_add_u64 v[6:7], s[6:7], 0, v[34:35]
	v_lshl_add_u64 v[6:7], v[6:7], 0, s[10:11]
	v_cmp_gt_i32_e32 vcc, s9, v37
	s_movk_i32 s9, 0xfa01
	v_and_b32_e32 v58, 63, v37
	v_cndmask_b32_e32 v4, v6, v4, vcc
	v_med3_i32 v6, v40, 1, v198
	v_cndmask_b32_e32 v5, v7, v5, vcc
	v_sub_u32_e32 v34, 0x800, v6
	global_load_dword v55, v[4:5], off
	v_lshl_add_u64 v[4:5], v[34:35], 2, s[6:7]
	v_lshlrev_b32_e32 v34, 2, v6
	v_lshl_add_u64 v[6:7], s[6:7], 0, v[34:35]
	v_lshl_add_u64 v[6:7], v[6:7], 0, s[10:11]
	v_cmp_gt_i32_e32 vcc, s9, v37
	s_nop 1
	v_cndmask_b32_e32 v4, v6, v4, vcc
	v_med3_i32 v6, v38, 1, v198
	v_cndmask_b32_e32 v5, v7, v5, vcc
	v_sub_u32_e32 v34, 0x800, v6
	global_load_dword v56, v[4:5], off
	v_lshl_add_u64 v[4:5], v[34:35], 2, s[6:7]
	v_lshlrev_b32_e32 v34, 2, v6
	v_lshl_add_u64 v[6:7], s[6:7], 0, v[34:35]
	s_movk_i32 s6, 0xf801
	v_lshl_add_u64 v[6:7], v[6:7], 0, s[10:11]
	v_cmp_gt_i32_e32 vcc, s6, v37
	v_add_u32_e32 v34, -1, v37
	s_movk_i32 s6, 0xfff
	v_cndmask_b32_e32 v5, v7, v5, vcc
	v_cndmask_b32_e32 v4, v6, v4, vcc
	v_add_co_u32_e32 v2, vcc, 0x4f000000, v2
	global_load_dword v57, v[4:5], off
	s_nop 0
	v_addc_co_u32_e32 v3, vcc, 0, v3, vcc
	global_load_dwordx4 v[26:29], v[158:159], off offset:64
	global_load_dwordx4 v[22:25], v[158:159], off offset:128
	global_load_dwordx4 v[18:21], v[158:159], off offset:192
	global_load_dwordx4 v[14:17], v[158:159], off offset:256
	global_load_dwordx4 v[10:13], v[158:159], off offset:320
	global_load_dwordx4 v[6:9], v[158:159], off offset:384
	global_load_dwordx4 v[30:33], v[2:3], off offset:512
	s_nop 0
	global_load_dwordx4 v[2:5], v[158:159], off offset:448
	v_cmp_gt_u32_e32 vcc, s6, v34
	s_waitcnt vmcnt(16)
	s_nop 0
	v_cndmask_b32_e32 v34, 0, v1, vcc
	v_add_u32_e32 v1, 0x1ff, v37
	v_cmp_gt_u32_e32 vcc, s6, v1
	s_waitcnt vmcnt(15)
	s_nop 0
	v_cndmask_b32_e32 v54, 0, v39, vcc
	v_add_u32_e32 v39, 0x3ff, v37
	v_cmp_gt_u32_e32 vcc, s6, v39
	v_add_u32_e32 v39, 0x5ff, v37
	v_add_f32_e64 v1, |v34|, |v54|
	s_waitcnt vmcnt(14)
	v_cndmask_b32_e32 v53, 0, v41, vcc
	v_cmp_gt_u32_e32 vcc, s6, v39
	v_add_u32_e32 v39, 0x7ff, v37
	v_add_f32_e64 v1, v1, |v53|
	s_waitcnt vmcnt(13)
	v_cndmask_b32_e32 v51, 0, v43, vcc
	v_cmp_gt_u32_e32 vcc, s6, v39
	v_add_u32_e32 v39, 0x9ff, v37
	v_add_f32_e64 v1, v1, |v51|
	s_waitcnt vmcnt(12)
	v_cndmask_b32_e32 v49, 0, v45, vcc
	v_cmp_gt_u32_e32 vcc, s6, v39
	v_add_u32_e32 v39, 0xbff, v37
	v_add_f32_e64 v1, v1, |v49|
	s_waitcnt vmcnt(11)
	v_cndmask_b32_e32 v47, 0, v47, vcc
	v_cmp_gt_u32_e32 vcc, s6, v39
	v_add_u32_e32 v39, 0xdff, v37
	v_add_f32_e64 v1, v1, |v47|
	s_waitcnt vmcnt(10)
	v_cndmask_b32_e32 v45, 0, v55, vcc
	v_cmp_gt_u32_e32 vcc, s6, v39
	v_add_f32_e64 v1, v1, |v45|
	s_waitcnt vmcnt(9)
	v_cndmask_b32_e32 v43, 0, v56, vcc
	v_cmp_lt_u32_e32 vcc, s31, v37
	v_add_f32_e64 v1, v1, |v43|
	s_waitcnt vmcnt(8)
	v_cndmask_b32_e32 v39, 0, v57, vcc
	v_add_f32_e64 v41, v1, |v39|
	v_ashrrev_i32_e32 v1, 6, v37
	v_cmp_eq_u32_e32 vcc, 0, v58
	v_add_f32_dpp v41, v41, v41 quad_perm:[1,0,3,2] row_mask:0xf bank_mask:0xf bound_ctrl:1
	s_nop 1
	v_add_f32_dpp v41, v41, v41 quad_perm:[2,3,0,1] row_mask:0xf bank_mask:0xf bound_ctrl:1
	s_nop 1
	v_add_f32_dpp v41, v41, v41 row_half_mirror row_mask:0xf bank_mask:0xf bound_ctrl:1
	s_nop 1
	v_add_f32_dpp v41, v41, v41 row_mirror row_mask:0xf bank_mask:0xf bound_ctrl:1
	s_nop 0
	v_readlane_b32 s14, v41, 0
	v_readlane_b32 s9, v41, 16
	v_readlane_b32 s15, v41, 32
	v_readlane_b32 s10, v41, 48
	s_and_saveexec_b64 s[6:7], vcc
	s_cbranch_execz .LBB0_2264
	v_mov_b32_e32 v56, s9
	v_mov_b32_e32 v57, s10
	v_lshl_add_u32 v41, v1, 2, 0
	v_pk_add_f32 v[56:57], s[14:15], v[56:57]
	v_add_u32_e32 v41, 0x10200, v41
	v_add_f32_e32 v55, v56, v57
	ds_write_b32 v41, v55

; __device__ __forceinline__ void ph_scan(CArgs& a, int l, LAS unsigned char* lds, int bid, int nblk, unsigned long long& tacc) {
;     ...
;     if (nblk == 256) {
;         if (bid < 128) hyena_unit<SEQ>(a, l, bid, lds);
;         else { const int g = bid - 128; hyena_unit<SEQ>(a, l, 128 + g, lds); if (l != DEPTH - 1) { hyena_unit<CTXL>(a, l, 2 * g, lds); hyena_unit<CTXL>(a, l, 2 * g + 1, lds); } }
.LBB0_2273:
	s_mov_b64 s[6:7], 0
	s_mov_b64 s[14:15], 0
	s_branch .LBB0_2494

; #define LAS __attribute__((address_space(3)))
; template <int L>
; __device__ __forceinline__ void hyena_unit(CArgs& a, int l, int c, LAS unsigned char* lds) {
;     ...
;         for (int ib = 0; ib < 8; ++ib) {
;             const bf16* zq = zp + 256 * (ib < 7 ? ib + 1 : 7);
; #pragma unroll
;             for (int ii = 0; ii < 8; ++ii) zn[ii] = *(const bf16x8*)(zq + 32 * ii);
; #pragma unroll
;             for (int ii = 0; ii < 8; ++ii) {
;                 A[(16 - 2 * ii) & 15] = *(const LAS bf16x8*)(ap + 64 * ii);
;                 A[(17 - 2 * ii) & 15] = *(const LAS bf16x8*)(ap + 64 * ii - 32);
; #pragma unroll
;                 for (int jj = 0; jj < 16; ++jj) { const int j = (jj + 2) & 15; acc[j] = __builtin_amdgcn_mfma_f32_16x16x32_bf16(A[(j + 16 - 2 * ii) & 15], zc[ii], acc[j], 0, 0, 0); }
;             }
;             ap += 512;
; #pragma unroll
;             for (int ii = 0; ii < 8; ++ii) zc[ii] = zn[ii];
;         }
.LBB0_2417:
	s_waitcnt vmcnt(1) lgkmcnt(1)
	s_nop 0
	v_mfma_f32_16x16x32_bf16 v[44:47], v[56:59], v[30:33], v[44:47]
	s_cmpk_lg_i32 s6, 0x800
	s_cselect_b32 s78, s6, 0x700
	s_addk_i32 s6, 0x100
	v_mfma_f32_16x16x32_bf16 v[36:39], v[80:83], v[30:33], v[36:39]
	s_cmpk_lg_i32 s6, 0x900
	v_mfma_f32_16x16x32_bf16 v[44:47], v[80:83], v[26:29], v[44:47]
	v_mfma_f32_16x16x32_bf16 v[136:139], v[88:91], v[30:33], v[136:139]
	v_mfma_f32_16x16x32_bf16 v[132:135], v[84:87], v[30:33], v[132:135]
	v_mfma_f32_16x16x32_bf16 v[128:131], v[104:107], v[30:33], v[128:131]
	v_mfma_f32_16x16x32_bf16 v[124:127], v[96:99], v[30:33], v[124:127]
	v_mfma_f32_16x16x32_bf16 v[48:51], v[112:115], v[30:33], v[48:51]
	v_mfma_f32_16x16x32_bf16 v[36:39], v[112:115], v[26:29], v[36:39]
	v_mfma_f32_16x16x32_bf16 v[44:47], v[112:115], v[22:25], v[44:47]
	v_subrev_u32_e32 v112, 32, v161
	s_waitcnt lgkmcnt(0)
	v_mfma_f32_16x16x32_bf16 v[52:55], v[60:63], v[30:33], v[52:55]
	v_mfma_f32_16x16x32_bf16 v[56:59], v[72:75], v[26:29], v[136:139]
	v_mfma_f32_16x16x32_bf16 v[60:63], v[68:71], v[26:29], v[132:135]
	s_nop 1
	ds_read_b128 v[136:139], v112
	ds_read_b128 v[132:135], v161
	v_mfma_f32_16x16x32_bf16 v[128:131], v[88:91], v[26:29], v[128:131]
	v_mfma_f32_16x16x32_bf16 v[124:127], v[84:87], v[26:29], v[124:127]
	v_mfma_f32_16x16x32_bf16 v[140:143], v[68:71], v[30:33], v[140:143]
	v_mfma_f32_16x16x32_bf16 v[40:43], v[76:79], v[30:33], v[40:43]
	v_mfma_f32_16x16x32_bf16 v[52:55], v[76:79], v[26:29], v[52:55]
	v_mfma_f32_16x16x32_bf16 v[76:79], v[72:75], v[22:25], v[128:131]
	v_mfma_f32_16x16x32_bf16 v[80:83], v[68:71], v[22:25], v[124:127]
	v_mfma_f32_16x16x32_bf16 v[144:147], v[72:75], v[30:33], v[144:147]
	s_waitcnt lgkmcnt(0)
	v_mfma_f32_16x16x32_bf16 v[124:127], v[132:135], v[22:25], v[56:59]
	v_mfma_f32_16x16x32_bf16 v[128:131], v[136:139], v[26:29], v[140:143]
	v_mfma_f32_16x16x32_bf16 v[140:143], v[136:139], v[22:25], v[60:63]
	s_nop 2
	ds_read_b128 v[60:63], v161 offset:64
	ds_read_b128 v[56:59], v161 offset:32
	v_mfma_f32_16x16x32_bf16 v[120:123], v[100:103], v[30:33], v[120:123]
	v_mfma_f32_16x16x32_bf16 v[92:95], v[108:111], v[30:33], v[92:95]
	v_mfma_f32_16x16x32_bf16 v[64:67], v[116:119], v[30:33], v[64:67]
	v_mfma_f32_16x16x32_bf16 v[40:43], v[116:119], v[26:29], v[40:43]
	v_mfma_f32_16x16x32_bf16 v[52:55], v[116:119], v[22:25], v[52:55]
	v_mfma_f32_16x16x32_bf16 v[112:115], v[132:135], v[30:33], v[148:151]
	v_mfma_f32_16x16x32_bf16 v[30:33], v[136:139], v[30:33], v[152:155]
	v_mfma_f32_16x16x32_bf16 v[76:79], v[132:135], v[18:21], v[76:79]
	v_mfma_f32_16x16x32_bf16 v[80:83], v[136:139], v[18:21], v[80:83]
	v_mfma_f32_16x16x32_bf16 v[116:119], v[132:135], v[26:29], v[144:147]
	v_mfma_f32_16x16x32_bf16 v[120:123], v[104:107], v[26:29], v[120:123]
	v_mfma_f32_16x16x32_bf16 v[92:95], v[96:99], v[26:29], v[92:95]
	v_mfma_f32_16x16x32_bf16 v[64:67], v[100:103], v[26:29], v[64:67]
	v_mfma_f32_16x16x32_bf16 v[48:51], v[108:111], v[26:29], v[48:51]
	v_mfma_f32_16x16x32_bf16 v[40:43], v[100:103], v[22:25], v[40:43]
	v_mfma_f32_16x16x32_bf16 v[52:55], v[100:103], v[18:21], v[52:55]
	s_waitcnt lgkmcnt(1)
	v_mfma_f32_16x16x32_bf16 v[100:103], v[60:63], v[26:29], v[112:115]
	v_mfma_f32_16x16x32_bf16 v[112:115], v[60:63], v[18:21], v[124:127]
	s_waitcnt lgkmcnt(0)
	v_mfma_f32_16x16x32_bf16 v[26:29], v[56:59], v[26:29], v[30:33]
	v_mfma_f32_16x16x32_bf16 v[30:33], v[56:59], v[22:25], v[128:131]
	v_mfma_f32_16x16x32_bf16 v[124:127], v[60:63], v[14:17], v[76:79]
	v_mfma_f32_16x16x32_bf16 v[128:131], v[56:59], v[14:17], v[80:83]
	s_nop 1
	ds_read_b128 v[76:79], v161 offset:128
	ds_read_b128 v[80:83], v161 offset:96
	v_mfma_f32_16x16x32_bf16 v[36:39], v[108:111], v[22:25], v[36:39]
	v_mfma_f32_16x16x32_bf16 v[44:47], v[108:111], v[18:21], v[44:47]
	v_mfma_f32_16x16x32_bf16 v[108:111], v[60:63], v[22:25], v[116:119]
	v_mfma_f32_16x16x32_bf16 v[116:119], v[56:59], v[18:21], v[140:143]
	v_mfma_f32_16x16x32_bf16 v[120:123], v[88:91], v[22:25], v[120:123]
	v_mfma_f32_16x16x32_bf16 v[92:95], v[84:87], v[22:25], v[92:95]
	v_mfma_f32_16x16x32_bf16 v[64:67], v[104:107], v[22:25], v[64:67]
	v_mfma_f32_16x16x32_bf16 v[48:51], v[96:99], v[22:25], v[48:51]
	v_mfma_f32_16x16x32_bf16 v[40:43], v[104:107], v[18:21], v[40:43]
	v_mfma_f32_16x16x32_bf16 v[36:39], v[96:99], v[18:21], v[36:39]
	v_mfma_f32_16x16x32_bf16 v[52:55], v[104:107], v[14:17], v[52:55]
	v_mfma_f32_16x16x32_bf16 v[44:47], v[96:99], v[14:17], v[44:47]
	s_waitcnt lgkmcnt(1)
	v_mfma_f32_16x16x32_bf16 v[96:99], v[76:79], v[22:25], v[100:103]
	v_mfma_f32_16x16x32_bf16 v[104:107], v[76:79], v[14:17], v[112:115]
	s_waitcnt lgkmcnt(0)
	v_mfma_f32_16x16x32_bf16 v[22:25], v[80:83], v[22:25], v[26:29]
	v_mfma_f32_16x16x32_bf16 v[26:29], v[80:83], v[18:21], v[30:33]
	v_mfma_f32_16x16x32_bf16 v[30:33], v[80:83], v[14:17], v[116:119]
	s_nop 2
	ds_read_b128 v[116:119], v161 offset:192
	ds_read_b128 v[112:115], v161 offset:160
	v_mfma_f32_16x16x32_bf16 v[100:103], v[76:79], v[18:21], v[108:111]
	v_mfma_f32_16x16x32_bf16 v[108:111], v[76:79], v[10:13], v[124:127]
	v_mfma_f32_16x16x32_bf16 v[124:127], v[80:83], v[10:13], v[128:131]
	v_mfma_f32_16x16x32_bf16 v[120:123], v[72:75], v[18:21], v[120:123]
	v_mfma_f32_16x16x32_bf16 v[92:95], v[68:71], v[18:21], v[92:95]
	v_mfma_f32_16x16x32_bf16 v[64:67], v[88:91], v[18:21], v[64:67]
	v_mfma_f32_16x16x32_bf16 v[48:51], v[84:87], v[18:21], v[48:51]
	v_mfma_f32_16x16x32_bf16 v[40:43], v[88:91], v[14:17], v[40:43]
	v_mfma_f32_16x16x32_bf16 v[36:39], v[84:87], v[14:17], v[36:39]
	v_mfma_f32_16x16x32_bf16 v[52:55], v[88:91], v[10:13], v[52:55]
	v_mfma_f32_16x16x32_bf16 v[44:47], v[84:87], v[10:13], v[44:47]
	s_waitcnt lgkmcnt(1)
; #define LAS __attribute__((address_space(3)))
; template <int L>
; __device__ __forceinline__ void hyena_unit(CArgs& a, int l, int c, LAS unsigned char* lds) {
;     ...
;         for (int ib = 0; ib < 8; ++ib) {
;             const bf16* zq = zp + 256 * (ib < 7 ? ib + 1 : 7);
; #pragma unroll
;             for (int ii = 0; ii < 8; ++ii) zn[ii] = *(const bf16x8*)(zq + 32 * ii);
; #pragma unroll
;             for (int ii = 0; ii < 8; ++ii) {
;                 A[(16 - 2 * ii) & 15] = *(const LAS bf16x8*)(ap + 64 * ii);
;                 A[(17 - 2 * ii) & 15] = *(const LAS bf16x8*)(ap + 64 * ii - 32);
; #pragma unroll
;                 for (int jj = 0; jj < 16; ++jj) { const int j = (jj + 2) & 15; acc[j] = __builtin_amdgcn_mfma_f32_16x16x32_bf16(A[(j + 16 - 2 * ii) & 15], zc[ii], acc[j], 0, 0, 0); }
;             }
;             ap += 512;
; #pragma unroll
;             for (int ii = 0; ii < 8; ++ii) zc[ii] = zn[ii];
;         }
	v_mfma_f32_16x16x32_bf16 v[84:87], v[116:119], v[18:21], v[96:99]
	v_mfma_f32_16x16x32_bf16 v[88:91], v[116:119], v[14:17], v[100:103]
	s_waitcnt lgkmcnt(0)
	v_mfma_f32_16x16x32_bf16 v[18:21], v[112:115], v[18:21], v[22:25]
	v_mfma_f32_16x16x32_bf16 v[22:25], v[112:115], v[14:17], v[26:29]
	v_mfma_f32_16x16x32_bf16 v[26:29], v[112:115], v[10:13], v[30:33]
	v_mfma_f32_16x16x32_bf16 v[30:33], v[116:119], v[6:9], v[108:111]
	ds_read_b128 v[100:103], v161 offset:256
	s_nop 1
	ds_read_b128 v[108:111], v161 offset:224
	v_mfma_f32_16x16x32_bf16 v[96:99], v[116:119], v[10:13], v[104:107]
	v_mfma_f32_16x16x32_bf16 v[104:107], v[112:115], v[6:9], v[124:127]
	v_mfma_f32_16x16x32_bf16 v[48:51], v[68:71], v[14:17], v[48:51]
	v_mfma_f32_16x16x32_bf16 v[36:39], v[68:71], v[10:13], v[36:39]
	v_mfma_f32_16x16x32_bf16 v[44:47], v[68:71], v[6:9], v[44:47]
	s_waitcnt lgkmcnt(1)
	v_mfma_f32_16x16x32_bf16 v[68:71], v[100:103], v[14:17], v[84:87]
	v_mfma_f32_16x16x32_bf16 v[84:87], v[100:103], v[6:9], v[96:99]
	s_waitcnt vmcnt(0) lgkmcnt(0)
	v_mfma_f32_16x16x32_bf16 v[124:127], v[108:111], v[2:5], v[104:107]
	s_nop 2
	ds_read_b128 v[104:107], v161 offset:320
	ds_read_b128 v[96:99], v161 offset:288
	v_mfma_f32_16x16x32_bf16 v[120:123], v[132:135], v[14:17], v[120:123]
	v_mfma_f32_16x16x32_bf16 v[92:95], v[136:139], v[14:17], v[92:95]
	v_mfma_f32_16x16x32_bf16 v[64:67], v[72:75], v[14:17], v[64:67]
	v_mfma_f32_16x16x32_bf16 v[14:17], v[108:111], v[14:17], v[18:21]
	v_mfma_f32_16x16x32_bf16 v[18:21], v[108:111], v[10:13], v[22:25]
	v_mfma_f32_16x16x32_bf16 v[22:25], v[108:111], v[6:9], v[26:29]
	s_waitcnt lgkmcnt(1)
	v_mfma_f32_16x16x32_bf16 v[26:29], v[104:107], v[10:13], v[68:71]
	s_nop 2
	v_lshl_add_u64 v[68:69], s[78:79], 1, v[158:159]
	v_mfma_f32_16x16x32_bf16 v[120:123], v[60:63], v[10:13], v[120:123]
	v_mfma_f32_16x16x32_bf16 v[92:95], v[56:59], v[10:13], v[92:95]
	v_mfma_f32_16x16x32_bf16 v[64:67], v[132:135], v[10:13], v[64:67]
	v_mfma_f32_16x16x32_bf16 v[48:51], v[136:139], v[10:13], v[48:51]
	v_mfma_f32_16x16x32_bf16 v[40:43], v[72:75], v[10:13], v[40:43]
	v_mfma_f32_16x16x32_bf16 v[52:55], v[72:75], v[6:9], v[52:55]
	v_mfma_f32_16x16x32_bf16 v[72:75], v[100:103], v[10:13], v[88:91]
	s_waitcnt lgkmcnt(0)
	v_mfma_f32_16x16x32_bf16 v[10:13], v[96:99], v[10:13], v[14:17]
	s_nop 2
	global_load_dwordx4 v[14:17], v[68:69], off
	v_mfma_f32_16x16x32_bf16 v[36:39], v[136:139], v[6:9], v[36:39]
	global_load_dwordx4 v[170:173], v[68:69], off offset:64
	global_load_dwordx4 v[174:177], v[68:69], off offset:128
	global_load_dwordx4 v[178:181], v[68:69], off offset:192
	v_mfma_f32_16x16x32_bf16 v[44:47], v[136:139], v[2:5], v[44:47]
	v_mfma_f32_16x16x32_bf16 v[136:139], v[104:107], v[2:5], v[84:87]
	ds_read_b128 v[88:91], v161 offset:384
	s_nop 1
	ds_read_b128 v[84:87], v161 offset:352
	global_load_dwordx4 v[182:185], v[68:69], off offset:256
	global_load_dwordx4 v[186:189], v[68:69], off offset:320
	global_load_dwordx4 v[202:205], v[68:69], off offset:384
	global_load_dwordx4 v[206:209], v[68:69], off offset:448
	v_mfma_f32_16x16x32_bf16 v[128:131], v[100:103], v[2:5], v[30:33]
	ds_read_b128 v[68:71], v161 offset:416
	v_mfma_f32_16x16x32_bf16 v[30:33], v[104:107], v[6:9], v[72:75]
	s_nop 2
	ds_read_b128 v[72:75], v161 offset:448
	v_mfma_f32_16x16x32_bf16 v[120:123], v[76:79], v[6:9], v[120:123]
	v_add_u32_e32 v161, 0x200, v161
	v_mfma_f32_16x16x32_bf16 v[92:95], v[80:83], v[6:9], v[92:95]
	v_mfma_f32_16x16x32_bf16 v[64:67], v[60:63], v[6:9], v[64:67]
	v_mfma_f32_16x16x32_bf16 v[48:51], v[56:59], v[6:9], v[48:51]
	v_mfma_f32_16x16x32_bf16 v[40:43], v[132:135], v[6:9], v[40:43]
	v_mfma_f32_16x16x32_bf16 v[52:55], v[132:135], v[2:5], v[52:55]
	v_mfma_f32_16x16x32_bf16 v[18:21], v[96:99], v[6:9], v[18:21]
	v_mfma_f32_16x16x32_bf16 v[132:135], v[96:99], v[2:5], v[22:25]
	s_waitcnt lgkmcnt(3)
	v_mfma_f32_16x16x32_bf16 v[22:25], v[88:91], v[6:9], v[26:29]
	s_waitcnt lgkmcnt(2)
	v_mfma_f32_16x16x32_bf16 v[6:9], v[84:87], v[6:9], v[10:13]
	s_waitcnt vmcnt(6)
	v_mov_b64_e32 v[26:27], v[170:171]
	v_mfma_f32_16x16x32_bf16 v[120:123], v[116:119], v[2:5], v[120:123]
	v_mov_b64_e32 v[28:29], v[172:173]
	s_waitcnt vmcnt(2)
	v_mov_b64_e32 v[10:11], v[186:187]
	v_mfma_f32_16x16x32_bf16 v[92:95], v[112:115], v[2:5], v[92:95]
	v_mov_b64_e32 v[12:13], v[188:189]
	v_mfma_f32_16x16x32_bf16 v[64:67], v[76:79], v[2:5], v[64:67]
	v_mfma_f32_16x16x32_bf16 v[48:51], v[80:83], v[2:5], v[48:51]
	v_mfma_f32_16x16x32_bf16 v[40:43], v[60:63], v[2:5], v[40:43]
	v_mfma_f32_16x16x32_bf16 v[36:39], v[56:59], v[2:5], v[36:39]
	v_mfma_f32_16x16x32_bf16 v[144:147], v[88:91], v[2:5], v[30:33]
	v_mfma_f32_16x16x32_bf16 v[140:143], v[84:87], v[2:5], v[18:21]
	s_nop 1
	v_mov_b64_e32 v[32:33], v[16:17]
	v_mov_b64_e32 v[30:31], v[14:15]
	v_mov_b64_e32 v[14:15], v[182:183]
	s_waitcnt lgkmcnt(0)
	v_mfma_f32_16x16x32_bf16 v[148:151], v[72:75], v[2:5], v[22:25]
	v_mov_b64_e32 v[18:19], v[178:179]
	v_mov_b64_e32 v[20:21], v[180:181]
	v_mov_b64_e32 v[16:17], v[184:185]
	v_mfma_f32_16x16x32_bf16 v[152:155], v[68:71], v[2:5], v[6:9]
	v_mov_b64_e32 v[22:23], v[174:175]
	s_waitcnt vmcnt(0)
	v_mov_b64_e32 v[2:3], v[206:207]
	v_mov_b64_e32 v[24:25], v[176:177]
	v_mov_b64_e32 v[6:7], v[202:203]
	v_mov_b64_e32 v[8:9], v[204:205]
	v_mov_b64_e32 v[4:5], v[208:209]
	s_cbranch_scc1 .LBB0_2417
; __device__ __forceinline__ unsigned pk2(float lo, float hi) { return f2bf(lo) | (f2bf(hi) << 16); }
; template <int L>
; __device__ __forceinline__ void hyena_unit(CArgs& a, int l, int c, LAS unsigned char* lds) {
;     ...
;     for (int j = 0; j < NTW; ++j) *(u32x2*)(YT + 16 * (w * NTW + j) + 4 * kg) = (u32x2){pk2(acc[j][0], acc[j][1]), pk2(acc[j][2], acc[j][3])};
;     __syncthreads();
; __device__ __forceinline__ void ph_scan(CArgs& a, int l, LAS unsigned char* lds, int bid, int nblk, unsigned long long& tacc) {
;     ...
;     if (nblk == 256) {
;         if (bid < 128) hyena_unit<SEQ>(a, l, bid, lds);
;         else { const int g = bid - 128; hyena_unit<SEQ>(a, l, 128 + g, lds); if (l != DEPTH - 1) { hyena_unit<CTXL>(a, l, 2 * g, lds); hyena_unit<CTXL>(a, l, 2 * g + 1, lds); } }
	v_lshlrev_b32_e32 v2, 8, v1
	v_cvt_pk_bf16_f32 v6, v148, v149
	v_lshl_add_u64 v[4:5], v[156:157], 0, v[34:35]
	v_cvt_pk_bf16_f32 v7, v150, v151
	v_ashrrev_i32_e32 v3, 31, v2
	v_lshl_add_u64 v[2:3], v[2:3], 1, v[4:5]
	s_mov_b64 s[6:7], 0x50400200
	v_lshl_add_u64 v[4:5], v[2:3], 0, s[6:7]
	s_mov_b32 s6, 0x50400000
	v_add_co_u32_e32 v2, vcc, s6, v2
	s_nop 0
	s_nop 0
	v_addc_co_u32_e32 v3, vcc, 0, v3, vcc
	global_store_dwordx2 v[2:3], v[6:7], off offset:512
	v_cvt_pk_bf16_f32 v2, v152, v153
	v_cvt_pk_bf16_f32 v3, v154, v155
	global_store_dwordx2 v[4:5], v[2:3], off offset:32
	v_cvt_pk_bf16_f32 v2, v144, v145
	v_cvt_pk_bf16_f32 v3, v146, v147
	global_store_dwordx2 v[4:5], v[2:3], off offset:64
	v_cvt_pk_bf16_f32 v2, v140, v141
	v_cvt_pk_bf16_f32 v3, v142, v143
	global_store_dwordx2 v[4:5], v[2:3], off offset:96
	v_cvt_pk_bf16_f32 v2, v136, v137
	v_cvt_pk_bf16_f32 v3, v138, v139
	global_store_dwordx2 v[4:5], v[2:3], off offset:128
	v_cvt_pk_bf16_f32 v2, v132, v133
	v_cvt_pk_bf16_f32 v3, v134, v135
	global_store_dwordx2 v[4:5], v[2:3], off offset:160
	v_cvt_pk_bf16_f32 v2, v128, v129
	v_cvt_pk_bf16_f32 v3, v130, v131
	global_store_dwordx2 v[4:5], v[2:3], off offset:192
	v_cvt_pk_bf16_f32 v2, v124, v125
	v_cvt_pk_bf16_f32 v3, v126, v127
	global_store_dwordx2 v[4:5], v[2:3], off offset:224
	v_cvt_pk_bf16_f32 v2, v120, v121
	v_cvt_pk_bf16_f32 v3, v122, v123
	global_store_dwordx2 v[4:5], v[2:3], off offset:256
	v_cvt_pk_bf16_f32 v2, v92, v93
	v_cvt_pk_bf16_f32 v3, v94, v95
	global_store_dwordx2 v[4:5], v[2:3], off offset:288
	v_cvt_pk_bf16_f32 v2, v64, v65
	v_cvt_pk_bf16_f32 v3, v66, v67
	global_store_dwordx2 v[4:5], v[2:3], off offset:320
	v_cvt_pk_bf16_f32 v2, v48, v49
	v_cvt_pk_bf16_f32 v3, v50, v51
	global_store_dwordx2 v[4:5], v[2:3], off offset:352
	v_cvt_pk_bf16_f32 v2, v40, v41
	v_cvt_pk_bf16_f32 v3, v42, v43
	global_store_dwordx2 v[4:5], v[2:3], off offset:384
	v_cvt_pk_bf16_f32 v2, v36, v37
	v_cvt_pk_bf16_f32 v3, v38, v39
	global_store_dwordx2 v[4:5], v[2:3], off offset:416
	v_cvt_pk_bf16_f32 v2, v52, v53
	v_cvt_pk_bf16_f32 v3, v54, v55
	global_store_dwordx2 v[4:5], v[2:3], off offset:448
	v_cvt_pk_bf16_f32 v2, v44, v45
	v_cvt_pk_bf16_f32 v1, v46, v46
	v_readlane_b32 s10, v250, 58
	v_lshrrev_b32_e32 v1, 16, v1
	v_cvt_pk_bf16_f32 v3, v47, v47
	v_readlane_b32 s11, v250, 59
	v_and_or_b32 v3, v3, s80, v1
	s_mov_b64 s[6:7], 0
	s_andn2_b64 vcc, exec, s[10:11]
	s_mov_b64 s[14:15], 0
	global_store_dwordx2 v[4:5], v[2:3], off offset:480
	s_barrier
	v_readlane_b32 s9, v252, 25
	s_lshl_b32 s16, s64, 4
	s_nop 1
	s_cmp_lg_u32 s9, s16
	s_cbranch_scc1 .Lhy2_done
	s_add_i32 s9, s16, 0xfffff800
	v_writelane_b32 v252, s9, 25
	s_add_i32 s9, s64, 0x180
	v_writelane_b32 v252, s9, 20
	s_branch .Lhy2_again
.Lhy2_done:
	v_writelane_b32 v252, s16, 25
	s_add_i32 s9, s64, 0x200
	v_writelane_b32 v252, s9, 20
	v_readlane_b32 s10, v250, 58
	v_readlane_b32 s11, v250, 59
	s_nop 1
	s_andn2_b64 vcc, exec, s[10:11]
	s_cbranch_vccnz .LBB0_2494
	v_readlane_b32 s9, v252, 21
	s_add_i32 s10, s8, s9
	v_mov_b32_e32 v38, v0
	s_ashr_i32 s11, s10, 31
	s_lshl_b64 s[10:11], s[10:11], 13
	v_and_b32_e32 v39, 15, v38
	v_readlane_b32 s9, v252, 22
	s_add_u32 s26, s2, 0x4f000000
	s_addc_u32 s27, s3, 0
	v_or_b32_e32 v1, s9, v39
	s_movk_i32 s9, 0x900
	v_mad_u64_u32 v[36:37], s[14:15], v1, s9, 0
	v_lshl_add_u64 v[2:3], v[36:37], 1, s[26:27]
	v_and_b32_e32 v34, 48, v38
	s_add_u32 s10, s0, s10
	v_med3_i32 v1, v38, 1, v197
	v_lshl_add_u64 v[2:3], v[2:3], 0, v[34:35]
	s_addc_u32 s11, s1, s11
	v_sub_u32_e32 v34, 0x100, v1
	v_lshl_add_u64 v[4:5], v[34:35], 2, s[10:11]
	v_lshlrev_b32_e32 v34, 2, v1
	v_lshl_add_u64 v[6:7], s[10:11], 0, v[34:35]
	s_mov_b64 s[14:15], 0x1ffc00
	s_movk_i32 s9, 0x101
	v_lshl_add_u64 v[6:7], v[6:7], 0, s[14:15]
	v_cmp_gt_i32_e32 vcc, s9, v38
	v_add_u32_e32 v40, 0x200, v38
	v_med3_i32 v1, v40, 1, v197
	v_cndmask_b32_e32 v5, v7, v5, vcc
	v_cndmask_b32_e32 v4, v6, v4, vcc
	global_load_dword v41, v[4:5], off
	v_sub_u32_e32 v34, 0x100, v1
	v_lshl_add_u64 v[4:5], v[34:35], 2, s[10:11]
	v_lshlrev_b32_e32 v34, 2, v1
	v_lshl_add_u64 v[6:7], s[10:11], 0, v[34:35]
	s_movk_i32 s9, 0xff01
	v_lshl_add_u64 v[6:7], v[6:7], 0, s[14:15]
	v_cmp_gt_i32_e32 vcc, s9, v38
	v_add_u32_e32 v34, -1, v38
	s_movk_i32 s9, 0x1ff
	v_cndmask_b32_e32 v5, v7, v5, vcc
	v_cndmask_b32_e32 v4, v6, v4, vcc
	global_load_dword v42, v[4:5], off
	global_load_dwordx4 v[30:33], v[2:3], off
	global_load_dwordx4 v[26:29], v[2:3], off offset:64
	global_load_dwordx4 v[22:25], v[2:3], off offset:128
	global_load_dwordx4 v[18:21], v[2:3], off offset:192
	global_load_dwordx4 v[14:17], v[2:3], off offset:256
	global_load_dwordx4 v[10:13], v[2:3], off offset:320
	global_load_dwordx4 v[6:9], v[2:3], off offset:384
	s_nop 0
	global_load_dwordx4 v[2:5], v[2:3], off offset:448
	v_cmp_gt_u32_e32 vcc, s9, v34
	v_and_b32_e32 v43, 63, v38
	v_ashrrev_i32_e32 v1, 6, v38
	s_waitcnt vmcnt(9)
	v_cndmask_b32_e32 v34, 0, v41, vcc
	v_cmp_lt_u32_e32 vcc, s30, v38
	s_waitcnt vmcnt(8)
	s_nop 0
	v_cndmask_b32_e32 v41, 0, v42, vcc
	v_add_f32_e64 v42, |v34|, |v41|
	v_cmp_eq_u32_e32 vcc, 0, v43
	s_nop 0
	v_add_f32_dpp v42, v42, v42 quad_perm:[1,0,3,2] row_mask:0xf bank_mask:0xf bound_ctrl:1
	s_nop 1
	v_add_f32_dpp v42, v42, v42 quad_perm:[2,3,0,1] row_mask:0xf bank_mask:0xf bound_ctrl:1
	s_nop 1
	v_add_f32_dpp v42, v42, v42 row_half_mirror row_mask:0xf bank_mask:0xf bound_ctrl:1
	s_nop 1
	v_add_f32_dpp v42, v42, v42 row_mirror row_mask:0xf bank_mask:0xf bound_ctrl:1
	s_nop 0
	v_readlane_b32 s28, v42, 0
	v_readlane_b32 s9, v42, 16
	v_readlane_b32 s29, v42, 32
	v_readlane_b32 s10, v42, 48
	s_and_saveexec_b64 s[14:15], vcc
	s_cbranch_execz .LBB0_2421
	v_mov_b32_e32 v42, s9
	v_mov_b32_e32 v43, s10
	v_pk_add_f32 v[42:43], s[28:29], v[42:43]
	v_lshl_add_u32 v44, v1, 2, 0
	v_add_f32_e32 v42, v42, v43
	ds_write_b32 v44, v42 offset:8704
